# v13: v12 + drop the L2-invalidating acquire fence after the panel-counter spin (exchange data is sc1-stored and sc1-loaded)
# speedup vs baseline: 1.0015x; 1.0015x over previous
;     __device__ __forceinline__ void fused(AccT& acc, const GUnit& u, int wr, int wc, int fr, int fq, LAS unsigned char* lds, int wid, int lane) const {
;     ...
;                 __builtin_amdgcn_fence(__ATOMIC_ACQUIRE, "agent");
;             }
;         }
;         asm volatile("s_waitcnt vmcnt(0) lgkmcnt(0)" ::: "memory"); __builtin_amdgcn_s_barrier(); asm volatile("" ::: "memory");
;         {
;             const int rowl = u.pn * 32 + (tid >> 4), e = tid & 15; float t[8], q[8];
; #pragma unroll
;             for (int k = 0; k < 8; ++k) t[k] = __hip_atomic_load(xlg + ((size_t)(u.pm * 8 + k) * 256 + rowl) * 16 + e, __ATOMIC_RELAXED, __HIP_MEMORY_SCOPE_AGENT);
;             if (lane < 32) {
;                 const int row = wid * 32 + lane;
; #pragma unroll
;                 for (int k = 0; k < 8; ++k) q[k] = __hip_atomic_load(xss + (size_t)(u.pm * 8 + k) * 256 + row, __ATOMIC_RELAXED, __HIP_MEMORY_SCOPE_AGENT);
;                 float ss = 0.f;
; #pragma unroll
;                 for (int k = 0; k < 8; ++k) ss += q[k];
;                 S[row] = 1.0f / sqrtf(ss * (1.f / DM) + EPS);
.LBB0_1295:
	s_waitcnt vmcnt(0)
.LBB0_1296:
	v_ashrrev_i32_e32 v79, 4, v79
	v_readlane_b32 s0, v255, 17
	v_lshlrev_b32_e32 v194, 2, v206
	s_ashr_i32 s41, s40, 31
	v_lshl_add_u32 v80, s0, 5, v79
	v_ashrrev_i32_e32 v81, 31, v80
	v_lshlrev_b64 v[92:93], 6, v[80:81]
	v_lshl_add_u64 v[92:93], s[42:43], 0, v[92:93]
	s_or_b32 s48, s40, 1
	v_lshl_add_u64 v[102:103], v[92:93], 0, v[194:195]
	s_lshl_b64 s[10:11], s[40:41], 14
	s_ashr_i32 s49, s48, 31
	s_or_b32 s50, s40, 2
	s_waitcnt vmcnt(0) lgkmcnt(0)
	s_barrier
	v_lshl_add_u64 v[92:93], v[102:103], 0, s[10:11]
	s_lshl_b64 s[10:11], s[48:49], 14
	s_ashr_i32 s51, s50, 31
	s_or_b32 s66, s40, 3
	global_load_dword v91, v[92:93], off sc1
	v_lshl_add_u64 v[92:93], v[102:103], 0, s[10:11]
	s_lshl_b64 s[10:11], s[50:51], 14
	s_ashr_i32 s67, s66, 31
	s_or_b32 s68, s40, 4
	v_lshl_add_u64 v[98:99], v[102:103], 0, s[10:11]
	s_lshl_b64 s[10:11], s[66:67], 14
	s_ashr_i32 s69, s68, 31
	s_or_b32 s70, s40, 5
	global_load_dword v92, v[92:93], off sc1
	s_ashr_i32 s71, s70, 31
	global_load_dword v93, v[98:99], off sc1
	v_lshl_add_u64 v[98:99], v[102:103], 0, s[10:11]
	s_lshl_b64 s[10:11], s[68:69], 14
	s_or_b32 s72, s40, 6
	v_lshl_add_u64 v[100:101], v[102:103], 0, s[10:11]
	s_lshl_b64 s[10:11], s[70:71], 14
	s_ashr_i32 s73, s72, 31
	s_or_b32 s74, s40, 7
	global_load_dword v99, v[98:99], off sc1
	s_ashr_i32 s75, s74, 31
	global_load_dword v98, v[100:101], off sc1
	v_lshl_add_u64 v[100:101], v[102:103], 0, s[10:11]
	s_lshl_b64 s[10:11], s[72:73], 14
	v_lshl_add_u64 v[104:105], v[102:103], 0, s[10:11]
	s_lshl_b64 s[10:11], s[74:75], 14
	v_lshl_add_u64 v[102:103], v[102:103], 0, s[10:11]
	global_load_dword v100, v[100:101], off sc1
	s_nop 0
	global_load_dword v101, v[104:105], off sc1
	s_nop 0
	global_load_dword v102, v[102:103], off sc1
	s_and_saveexec_b64 s[42:43], s[34:35]
	s_cbranch_execz .LBB0_1298
	v_ashrrev_i32_e32 v79, 31, v78
	v_lshl_add_u64 v[104:105], v[78:79], 2, s[12:13]
	s_lshl_b64 s[10:11], s[40:41], 10
	v_lshl_add_u64 v[110:111], v[104:105], 0, s[10:11]
	s_lshl_b64 s[10:11], s[48:49], 10
	global_load_dword v79, v[110:111], off sc1
	v_lshl_add_u64 v[110:111], v[104:105], 0, s[10:11]
	s_lshl_b64 s[10:11], s[50:51], 10
	global_load_dword v103, v[110:111], off sc1
	v_lshl_add_u64 v[110:111], v[104:105], 0, s[10:11]
	s_lshl_b64 s[10:11], s[66:67], 10
	global_load_dword v112, v[110:111], off sc1
	v_lshl_add_u64 v[110:111], v[104:105], 0, s[10:11]
	s_lshl_b64 s[10:11], s[68:69], 10
	global_load_dword v113, v[110:111], off sc1
	v_lshl_add_u64 v[110:111], v[104:105], 0, s[10:11]
	s_lshl_b64 s[10:11], s[70:71], 10
	global_load_dword v118, v[110:111], off sc1
	v_lshl_add_u64 v[110:111], v[104:105], 0, s[10:11]
	s_lshl_b64 s[10:11], s[72:73], 10
	global_load_dword v119, v[110:111], off sc1
	v_lshl_add_u64 v[110:111], v[104:105], 0, s[10:11]
	s_lshl_b64 s[10:11], s[74:75], 10
	global_load_dword v110, v[110:111], off sc1
	v_lshl_add_u64 v[104:105], v[104:105], 0, s[10:11]
	global_load_dword v104, v[104:105], off sc1
	v_lshl_add_u32 v78, v78, 2, 0
	s_waitcnt vmcnt(7)
	v_add_f32_e32 v79, 0, v79
	s_waitcnt vmcnt(6)
	v_add_f32_e32 v79, v79, v103
	s_waitcnt vmcnt(5)
	v_add_f32_e32 v79, v79, v112
	s_waitcnt vmcnt(4)
	v_add_f32_e32 v79, v79, v113
	s_waitcnt vmcnt(3)
	v_add_f32_e32 v79, v79, v118
	s_waitcnt vmcnt(2)
	v_add_f32_e32 v79, v79, v119
	s_waitcnt vmcnt(1)
	v_add_f32_e32 v79, v79, v110
	s_waitcnt vmcnt(0)
	v_add_f32_e32 v79, v79, v104
	v_fmamk_f32 v79, v79, 0x3a000000, v217
	v_mul_f32_e32 v103, 0x4f800000, v79
	v_cmp_gt_f32_e32 vcc, s5, v79
	s_nop 1
	v_cndmask_b32_e32 v79, v79, v103, vcc
	v_sqrt_f32_e32 v103, v79
	s_nop 0
	v_add_u32_e32 v104, -1, v103
	v_add_u32_e32 v105, 1, v103
	v_fma_f32 v110, -v104, v103, v79
	v_fma_f32 v111, -v105, v103, v79
	v_cmp_ge_f32_e64 s[34:35], 0, v110
	s_nop 1
	v_cndmask_b32_e64 v103, v103, v104, s[34:35]
	v_cmp_lt_f32_e64 s[34:35], 0, v111
	s_nop 1
	v_cndmask_b32_e64 v103, v103, v105, s[34:35]
	v_mul_f32_e32 v104, 0x37800000, v103
	v_cndmask_b32_e32 v103, v103, v104, vcc
	v_cmp_class_f32_e32 vcc, v79, v219
	s_nop 1
	v_cndmask_b32_e32 v79, v103, v79, vcc
	v_div_scale_f32 v103, s[10:11], v79, v79, 1.0
	v_rcp_f32_e32 v104, v103
	v_div_scale_f32 v105, vcc, 1.0, v79, 1.0
	v_fma_f32 v110, -v103, v104, 1.0
	v_fmac_f32_e32 v104, v110, v104
	v_mul_f32_e32 v110, v105, v104
	v_fma_f32 v111, -v103, v110, v105
	v_fmac_f32_e32 v110, v111, v104
	v_fma_f32 v103, -v103, v110, v105
	v_div_fmas_f32 v103, v103, v104, v110
	v_div_fixup_f32 v79, v103, v79, 1.0
	ds_write_b32 v78, v79 offset:4096
